# W1 conversion split by XCD parity (blockIdx bit0) instead of blockIdx bit3
# speedup vs baseline: 1.0064x; 1.0064x over previous
; #define LAS __attribute__((address_space(3)))
; #define REP(n) for (int rep_ = 0; rep_ < 1 + ((REPMASK >> (n)) & 1); ++rep_)
; #define IN(k) (lo <= (k) && (k) < hi && ((F = make_frame((LAS unsigned char*)lds_raw, wv)), true))
; #define SEAM(k) do { if ((k) + 1 < hi) xcd_barrier(bar, tid_now(wv) == 0); } while (0)
; DI void phase_expert_weights(const Frame& F, int l, int which) {
;     LAS float* scr = (LAS float*)(F.lds + F.wave * 16384);
;     unsigned char* ws = F.ws;
;     if (which == 0) {
;         constexpr int IPM = (D / 64) * (2048 / 32);
;         for (int it = F.gw; it < NE * IPM; it += F.NGW) { const int mtx = l * NE + it / IPM, r = it % IPM;
;             transpose_item(F.ap->in[32] + (size_t)mtx * D * 2048, D, 2048, (bf16_t*)(ws + WS_W1 + (size_t)mtx * 2048 * D), 3, scr, r, F.lane); }
; __global__ void __launch_bounds__(NTHR, 2) fwd_kernel(Args args) {
;     ...
;         REP(11) if (PM(11)) if (IN(pb + 8)) { phase_tail(F, l); SEAM(pb + 8); }
;         if (IN(pb + 9)) { phase_expert_weights(F, l, 0); SEAM(pb + 9); }
.LBB0_951:
	v_readlane_b32 s8, v253, 56
	v_readlane_b32 s9, v253, 57
	s_cmp_gt_i32 s96, s17
	s_mov_b32 s9, s29
	s_cselect_b64 s[4:5], -1, 0
	s_lshl_b32 s28, s8, 5
	v_writelane_b32 v253, s8, 56
	s_xor_b64 s[6:7], s[38:39], -1
	s_lshl_b64 s[48:49], s[8:9], 3
	v_writelane_b32 v253, s9, 57
	s_nop 0
	v_readlane_b32 s2, v253, 58
	s_or_b32 s17, s2, 11
	s_cmp_lt_i32 s17, s97
	s_cselect_b64 s[50:51], -1, 0
	s_or_b64 s[4:5], s[4:5], s[6:7]
	s_and_b64 vcc, exec, s[4:5]
	s_cbranch_vccnz .LBB0_1102
	s_bitcmp0_b32 s94, 0
	s_cbranch_scc1 .Lpre_skip
	s_mov_b32 s22, s10
	s_mov_b32 s23, s17
	s_mov_b64 s[24:25], s[38:39]
	v_mov_b32_e32 v42, v17
	s_mov_b64 s[4:5], s[58:59]
	v_readlane_b32 s2, v252, 0
	s_waitcnt lgkmcnt(0)
	v_mbcnt_lo_u32_b32 v0, -1, 0
	v_mbcnt_hi_u32_b32 v0, -1, v0
	s_mov_b32 s6, s94
	v_add_u32_e32 v1, s2, v0
	s_mov_b32 s2, s60
	s_and_b32 s7, s2, 7
	s_cmp_lg_u32 s7, 0
	v_readfirstlane_b32 s7, v1
	s_cbranch_scc1 .Lpre_1107
	s_ashr_i32 s9, s6, 31
	s_lshr_b32 s9, s9, 29
	s_add_i32 s9, s6, s9
	s_ashr_i32 s10, s9, 3
	s_and_b32 s9, s9, -8
	s_ashr_i32 s8, s2, 3
	s_sub_i32 s6, s6, s9
	s_mul_i32 s6, s8, s6
	s_add_i32 s6, s6, s10

; #define LAS __attribute__((address_space(3)))
; DI void phase_expert_weights(const Frame& F, int l, int which) {
;     LAS float* scr = (LAS float*)(F.lds + F.wave * 16384);
;     unsigned char* ws = F.ws;
;     if (which == 0) {
;         constexpr int IPM = (D / 64) * (2048 / 32);
;         for (int it = F.gw; it < NE * IPM; it += F.NGW) { const int mtx = l * NE + it / IPM, r = it % IPM;
;             transpose_item(F.ap->in[32] + (size_t)mtx * D * 2048, D, 2048, (bf16_t*)(ws + WS_W1 + (size_t)mtx * 2048 * D), 3, scr, r, F.lane); }
.LBB0_1104:
	v_readlane_b32 s50, v253, 50
	s_andn2_b64 vcc, exec, s[4:5]
	v_readlane_b32 s51, v253, 51
	s_cbranch_vccnz .LBB0_1160
	s_bitcmp1_b32 s94, 0
	s_cbranch_scc1 .LBB0_1110
	s_mov_b64 s[4:5], s[58:59]
	v_readlane_b32 s2, v252, 0
	s_waitcnt lgkmcnt(0)
	v_mbcnt_lo_u32_b32 v0, -1, 0
	v_mbcnt_hi_u32_b32 v0, -1, v0
	s_mov_b32 s6, s94
	v_add_u32_e32 v1, s2, v0
	s_mov_b32 s2, s60
	s_and_b32 s7, s2, 7
	s_cmp_lg_u32 s7, 0
	v_readfirstlane_b32 s7, v1
	s_cbranch_scc1 .LBB0_1107
	s_ashr_i32 s9, s6, 31
	s_lshr_b32 s9, s9, 29
	s_add_i32 s9, s6, s9
	s_ashr_i32 s10, s9, 3
	s_and_b32 s9, s9, -8
	s_ashr_i32 s8, s2, 3
	s_sub_i32 s6, s6, s9
	s_mul_i32 s6, s8, s6
	s_add_i32 s6, s6, s10
